# P23: wave halves keep their one-barrier offset across units (per-unit re-alignment barrier pair removed; epilogue has no barrier / LDS use)
# speedup vs baseline: 1.0015x; 1.0015x over previous
.Lh23_last:
	v_mov_b32_e32 v172, v177
	ds_read_b128 v[164:167], v196 offset:49152
	ds_read_b128 v[168:171], v196 offset:50176
	ds_read_b128 v[198:201], v196 offset:51200
	ds_read_b128 v[202:205], v196 offset:52224
	ds_read_b128 v[214:217], v196 offset:53248
	ds_read_b128 v[218:221], v196 offset:54272
	ds_read_b128 v[222:225], v196 offset:55296
	ds_read_b128 v[226:229], v196 offset:56320
	s_mov_b32 m0, s58
	v_add_u32_e32 v172, s85, v172
	global_load_lds_dwordx4 v172, s[6:7]
	v_mov_b32_e32 v172, v177
	s_add_i32 s85, s85, s48
	v_add_u32_e32 v172, s85, v172
	s_mov_b32 m0, s59
	s_add_i32 s85, s85, s48
	global_load_lds_dwordx4 v172, s[6:7]
	v_mov_b32_e32 v172, v177
	s_mov_b32 m0, s62
	v_add_u32_e32 v172, s85, v172
	global_load_lds_dwordx4 v172, s[6:7]
	v_mov_b32_e32 v172, v177
	s_add_i32 s85, s85, s48
	v_add_u32_e32 v172, s85, v172
	s_mov_b32 m0, s63
	s_nop 0
	global_load_lds_dwordx4 v172, s[6:7]
	v_mov_b32_e32 v172, v176
	s_mov_b32 m0, s60
	v_add_u32_e32 v172, s84, v172
	global_load_lds_dwordx4 v172, s[4:5]
	v_mov_b32_e32 v172, v176
	s_add_i32 s84, s84, s47
	v_add_u32_e32 v172, s84, v172
	s_mov_b32 m0, s61
	s_nop 0
	global_load_lds_dwordx4 v172, s[4:5]
	s_mul_hi_i32 s25, s81, 0x2e8ba2e9
	s_lshr_b32 s28, s25, 31
	s_lshr_b32 s25, s25, 3
	s_add_i32 s25, s25, s28
	s_mul_i32 s25, s25, 44
	s_sub_i32 s25, s81, s25
	s_lshl_b32 s28, s25, 7
	s_lshl_b32 s24, s24, 8
	s_add_i32 s24, s24, s66
	s_mul_i32 s24, s24, s71
	s_add_i32 s24, s24, s28
	s_add_i32 s24, s24, s8
	s_add_u32 s100, s12, s24
	s_addc_u32 s101, s13, 0
	s_mov_b32 s98, 0xbfb8aa3b
	v_mul_u32_u24_e32 v206, s71, v178
	v_lshl_add_u32 v206, v179, 3, v206
	v_pk_fma_f32 v[158:159], v[158:159], s[18:19], 0 op_sel_hi:[1,0,0]
	v_pk_fma_f32 v[160:161], v[160:161], s[18:19], 0 op_sel_hi:[1,0,0]
	v_pk_fma_f32 v[154:155], v[154:155], s[18:19], 0 op_sel_hi:[1,0,0]
	v_pk_fma_f32 v[156:157], v[156:157], s[18:19], 0 op_sel_hi:[1,0,0]
	v_pk_fma_f32 v[142:143], v[142:143], s[20:21], 0 op_sel_hi:[1,0,0]
	v_pk_fma_f32 v[144:145], v[144:145], s[20:21], 0 op_sel_hi:[1,0,0]
	v_pk_fma_f32 v[134:135], v[134:135], s[20:21], 0 op_sel_hi:[1,0,0]
	v_pk_fma_f32 v[136:137], v[136:137], s[20:21], 0 op_sel_hi:[1,0,0]
	v_pk_fma_f32 v[150:151], v[150:151], s[18:19], 0 op_sel_hi:[1,0,0]
	v_pk_fma_f32 v[152:153], v[152:153], s[18:19], 0 op_sel_hi:[1,0,0]
	v_pk_fma_f32 v[146:147], v[146:147], s[18:19], 0 op_sel_hi:[1,0,0]
	v_pk_fma_f32 v[148:149], v[148:149], s[18:19], 0 op_sel_hi:[1,0,0]
	v_pk_fma_f32 v[126:127], v[126:127], s[20:21], 0 op_sel_hi:[1,0,0]
	v_pk_fma_f32 v[128:129], v[128:129], s[20:21], 0 op_sel_hi:[1,0,0]
	v_pk_fma_f32 v[118:119], v[118:119], s[20:21], 0 op_sel_hi:[1,0,0]
	v_pk_fma_f32 v[120:121], v[120:121], s[20:21], 0 op_sel_hi:[1,0,0]
	v_pk_mul_f32 v[230:231], v[158:159], s[98:99] op_sel_hi:[1,0]
	v_pk_mul_f32 v[232:233], v[160:161], s[98:99] op_sel_hi:[1,0]
	v_pk_mul_f32 v[234:235], v[154:155], s[98:99] op_sel_hi:[1,0]
	v_pk_mul_f32 v[236:237], v[156:157], s[98:99] op_sel_hi:[1,0]
	v_pk_mul_f32 v[238:239], v[150:151], s[98:99] op_sel_hi:[1,0]
	v_pk_mul_f32 v[240:241], v[152:153], s[98:99] op_sel_hi:[1,0]
	v_pk_mul_f32 v[242:243], v[146:147], s[98:99] op_sel_hi:[1,0]
	v_pk_mul_f32 v[244:245], v[148:149], s[98:99] op_sel_hi:[1,0]
	v_exp_f32_e32 v230, v230
	v_exp_f32_e32 v231, v231
	v_exp_f32_e32 v232, v232
	v_exp_f32_e32 v233, v233
	v_exp_f32_e32 v234, v234
	v_exp_f32_e32 v235, v235
	v_exp_f32_e32 v236, v236
	v_exp_f32_e32 v237, v237
	v_exp_f32_e32 v238, v238
	v_exp_f32_e32 v239, v239
	v_exp_f32_e32 v240, v240
	v_exp_f32_e32 v241, v241
	v_exp_f32_e32 v242, v242
	v_exp_f32_e32 v243, v243
	v_exp_f32_e32 v244, v244
	v_exp_f32_e32 v245, v245
	v_pk_add_f32 v[230:231], v[230:231], 1.0 op_sel_hi:[1,0]
	v_pk_add_f32 v[232:233], v[232:233], 1.0 op_sel_hi:[1,0]
	v_pk_add_f32 v[234:235], v[234:235], 1.0 op_sel_hi:[1,0]
	v_pk_add_f32 v[236:237], v[236:237], 1.0 op_sel_hi:[1,0]
	v_pk_add_f32 v[238:239], v[238:239], 1.0 op_sel_hi:[1,0]
	v_pk_add_f32 v[240:241], v[240:241], 1.0 op_sel_hi:[1,0]
	v_pk_add_f32 v[242:243], v[242:243], 1.0 op_sel_hi:[1,0]
	v_pk_add_f32 v[244:245], v[244:245], 1.0 op_sel_hi:[1,0]
	v_rcp_f32_e32 v230, v230
	v_rcp_f32_e32 v231, v231
	v_rcp_f32_e32 v232, v232
	v_rcp_f32_e32 v233, v233
	v_rcp_f32_e32 v234, v234
	v_rcp_f32_e32 v235, v235
	v_rcp_f32_e32 v236, v236
	v_rcp_f32_e32 v237, v237
	v_rcp_f32_e32 v238, v238
	v_rcp_f32_e32 v239, v239
	v_rcp_f32_e32 v240, v240
	v_rcp_f32_e32 v241, v241
	v_rcp_f32_e32 v242, v242
	v_rcp_f32_e32 v243, v243
	v_rcp_f32_e32 v244, v244
	v_rcp_f32_e32 v245, v245
	v_pk_mul_f32 v[230:231], v[158:159], v[230:231]
	v_pk_mul_f32 v[232:233], v[160:161], v[232:233]
	v_pk_mul_f32 v[234:235], v[154:155], v[234:235]
	v_pk_mul_f32 v[236:237], v[156:157], v[236:237]
	v_pk_mul_f32 v[238:239], v[150:151], v[238:239]
	v_pk_mul_f32 v[240:241], v[152:153], v[240:241]
	v_pk_mul_f32 v[242:243], v[146:147], v[242:243]
	v_pk_mul_f32 v[244:245], v[148:149], v[244:245]
	v_pk_mul_f32 v[142:143], v[142:143], v[230:231]
	v_pk_mul_f32 v[144:145], v[144:145], v[232:233]
	v_pk_mul_f32 v[134:135], v[134:135], v[234:235]
	v_pk_mul_f32 v[136:137], v[136:137], v[236:237]
	v_pk_mul_f32 v[126:127], v[126:127], v[238:239]
	v_pk_mul_f32 v[128:129], v[128:129], v[240:241]
	v_pk_mul_f32 v[118:119], v[118:119], v[242:243]
	v_pk_mul_f32 v[120:121], v[120:121], v[244:245]
	v_med3_f32 v142, v142, s72, v197
	v_med3_f32 v143, v143, s72, v197
	v_med3_f32 v144, v144, s72, v197
	v_med3_f32 v145, v145, s72, v197
	v_med3_f32 v134, v134, s72, v197
	v_med3_f32 v135, v135, s72, v197
	v_med3_f32 v136, v136, s72, v197
	v_med3_f32 v137, v137, s72, v197
	v_med3_f32 v126, v126, s72, v197
	v_med3_f32 v127, v127, s72, v197
	v_med3_f32 v128, v128, s72, v197
	v_med3_f32 v129, v129, s72, v197
	v_med3_f32 v118, v118, s72, v197
	v_med3_f32 v119, v119, s72, v197
	v_med3_f32 v120, v120, s72, v197
	v_med3_f32 v121, v121, s72, v197
	v_cvt_pk_fp8_f32 v246, v142, v143
	v_cvt_pk_fp8_f32 v247, v134, v135
	v_cvt_pk_fp8_f32 v248, v126, v127
	v_cvt_pk_fp8_f32 v249, v118, v119
	v_add_u32_e32 v208, s57, v206
	v_cvt_pk_fp8_f32 v246, v144, v145 op_sel:[0,0,1]
	v_cvt_pk_fp8_f32 v247, v136, v137 op_sel:[0,0,1]
	v_cvt_pk_fp8_f32 v248, v128, v129 op_sel:[0,0,1]
	v_cvt_pk_fp8_f32 v249, v120, v121 op_sel:[0,0,1]
	s_nop 1
	global_store_dwordx2 v206, v[246:247], s[100:101]
	global_store_dwordx2 v208, v[248:249], s[100:101]
	s_waitcnt vmcnt(10)
	s_waitcnt lgkmcnt(0)
	s_barrier
	s_setprio 1
	s_waitcnt lgkmcnt(0)
	v_mfma_f32_16x16x128_f8f6f4 v[94:97], v[2:9], v[164:171], v[94:97]
	v_pk_fma_f32 v[138:139], v[138:139], s[18:19], 0 op_sel_hi:[1,0,0]
	v_pk_fma_f32 v[140:141], v[140:141], s[18:19], 0 op_sel_hi:[1,0,0]
	v_pk_fma_f32 v[130:131], v[130:131], s[18:19], 0 op_sel_hi:[1,0,0]
	v_pk_fma_f32 v[132:133], v[132:133], s[18:19], 0 op_sel_hi:[1,0,0]
	v_pk_fma_f32 v[110:111], v[110:111], s[20:21], 0 op_sel_hi:[1,0,0]
	v_pk_fma_f32 v[112:113], v[112:113], s[20:21], 0 op_sel_hi:[1,0,0]
	v_pk_fma_f32 v[106:107], v[106:107], s[20:21], 0 op_sel_hi:[1,0,0]
	v_mfma_f32_16x16x128_f8f6f4 v[90:93], v[10:17], v[164:171], v[90:93]
	v_pk_fma_f32 v[108:109], v[108:109], s[20:21], 0 op_sel_hi:[1,0,0]
	v_pk_fma_f32 v[122:123], v[122:123], s[18:19], 0 op_sel_hi:[1,0,0]
	v_pk_fma_f32 v[124:125], v[124:125], s[18:19], 0 op_sel_hi:[1,0,0]
	v_pk_fma_f32 v[114:115], v[114:115], s[18:19], 0 op_sel_hi:[1,0,0]
	v_pk_fma_f32 v[116:117], v[116:117], s[18:19], 0 op_sel_hi:[1,0,0]
	v_pk_fma_f32 v[102:103], v[102:103], s[20:21], 0 op_sel_hi:[1,0,0]
	v_pk_fma_f32 v[104:105], v[104:105], s[20:21], 0 op_sel_hi:[1,0,0]
	v_mfma_f32_16x16x128_f8f6f4 v[86:89], v[2:9], v[198:205], v[86:89]
	v_pk_fma_f32 v[98:99], v[98:99], s[20:21], 0 op_sel_hi:[1,0,0]
	v_pk_fma_f32 v[100:101], v[100:101], s[20:21], 0 op_sel_hi:[1,0,0]
	v_pk_mul_f32 v[230:231], v[138:139], s[98:99] op_sel_hi:[1,0]
	v_pk_mul_f32 v[232:233], v[140:141], s[98:99] op_sel_hi:[1,0]
	v_pk_mul_f32 v[234:235], v[130:131], s[98:99] op_sel_hi:[1,0]
	v_pk_mul_f32 v[236:237], v[132:133], s[98:99] op_sel_hi:[1,0]
	v_pk_mul_f32 v[238:239], v[122:123], s[98:99] op_sel_hi:[1,0]
	v_mfma_f32_16x16x128_f8f6f4 v[82:85], v[10:17], v[198:205], v[82:85]
	v_pk_mul_f32 v[240:241], v[124:125], s[98:99] op_sel_hi:[1,0]
	v_pk_mul_f32 v[242:243], v[114:115], s[98:99] op_sel_hi:[1,0]
	v_pk_mul_f32 v[244:245], v[116:117], s[98:99] op_sel_hi:[1,0]
	v_exp_f32_e32 v230, v230
	v_exp_f32_e32 v231, v231
	v_exp_f32_e32 v232, v232
	v_exp_f32_e32 v233, v233
	v_mfma_f32_16x16x128_f8f6f4 v[74:77], v[2:9], v[214:221], v[74:77]
	v_exp_f32_e32 v234, v234
	v_exp_f32_e32 v235, v235
	v_exp_f32_e32 v236, v236
	v_exp_f32_e32 v237, v237
	v_exp_f32_e32 v238, v238
	v_exp_f32_e32 v239, v239
	v_exp_f32_e32 v240, v240
	v_mfma_f32_16x16x128_f8f6f4 v[66:69], v[10:17], v[214:221], v[66:69]
	v_exp_f32_e32 v241, v241
	v_exp_f32_e32 v242, v242
	v_exp_f32_e32 v243, v243
	v_exp_f32_e32 v244, v244
	v_exp_f32_e32 v245, v245
	v_pk_add_f32 v[230:231], v[230:231], 1.0 op_sel_hi:[1,0]
	v_pk_add_f32 v[232:233], v[232:233], 1.0 op_sel_hi:[1,0]
	v_mfma_f32_16x16x128_f8f6f4 v[58:61], v[2:9], v[222:229], v[58:61]
	v_pk_add_f32 v[234:235], v[234:235], 1.0 op_sel_hi:[1,0]
	v_pk_add_f32 v[236:237], v[236:237], 1.0 op_sel_hi:[1,0]
	v_pk_add_f32 v[238:239], v[238:239], 1.0 op_sel_hi:[1,0]
	v_pk_add_f32 v[240:241], v[240:241], 1.0 op_sel_hi:[1,0]
	v_pk_add_f32 v[242:243], v[242:243], 1.0 op_sel_hi:[1,0]
	v_pk_add_f32 v[244:245], v[244:245], 1.0 op_sel_hi:[1,0]
	v_rcp_f32_e32 v230, v230
	v_mfma_f32_16x16x128_f8f6f4 v[50:53], v[10:17], v[222:229], v[50:53]
	v_rcp_f32_e32 v231, v231
	v_rcp_f32_e32 v232, v232
	v_rcp_f32_e32 v233, v233
	v_rcp_f32_e32 v234, v234
	v_rcp_f32_e32 v235, v235
	v_rcp_f32_e32 v236, v236
	v_rcp_f32_e32 v237, v237
	s_setprio 0
	s_setprio 1
	v_mfma_f32_16x16x128_f8f6f4 v[78:81], v[18:25], v[164:171], v[78:81]
	v_rcp_f32_e32 v238, v238
	v_rcp_f32_e32 v239, v239
	v_rcp_f32_e32 v240, v240
	v_rcp_f32_e32 v241, v241
	v_rcp_f32_e32 v242, v242
	v_rcp_f32_e32 v243, v243
	v_rcp_f32_e32 v244, v244
	v_mfma_f32_16x16x128_f8f6f4 v[70:73], v[26:33], v[164:171], v[70:73]
	v_rcp_f32_e32 v245, v245
	v_pk_mul_f32 v[230:231], v[138:139], v[230:231]
	v_pk_mul_f32 v[232:233], v[140:141], v[232:233]
	v_pk_mul_f32 v[234:235], v[130:131], v[234:235]
	v_pk_mul_f32 v[236:237], v[132:133], v[236:237]
	v_pk_mul_f32 v[238:239], v[122:123], v[238:239]
	v_pk_mul_f32 v[240:241], v[124:125], v[240:241]
	v_mfma_f32_16x16x128_f8f6f4 v[62:65], v[18:25], v[198:205], v[62:65]
	v_pk_mul_f32 v[242:243], v[114:115], v[242:243]
	v_pk_mul_f32 v[244:245], v[116:117], v[244:245]
	v_pk_mul_f32 v[110:111], v[110:111], v[230:231]
	v_pk_mul_f32 v[112:113], v[112:113], v[232:233]
	v_pk_mul_f32 v[106:107], v[106:107], v[234:235]
	v_pk_mul_f32 v[108:109], v[108:109], v[236:237]
	v_pk_mul_f32 v[102:103], v[102:103], v[238:239]
	v_mfma_f32_16x16x128_f8f6f4 v[54:57], v[26:33], v[198:205], v[54:57]
	v_pk_mul_f32 v[104:105], v[104:105], v[240:241]
	v_pk_mul_f32 v[98:99], v[98:99], v[242:243]
	v_pk_mul_f32 v[100:101], v[100:101], v[244:245]
	v_med3_f32 v110, v110, s72, v197
	v_med3_f32 v111, v111, s72, v197
	v_med3_f32 v112, v112, s72, v197
	v_med3_f32 v113, v113, s72, v197
	v_mfma_f32_16x16x128_f8f6f4 v[46:49], v[18:25], v[214:221], v[46:49]
	v_med3_f32 v106, v106, s72, v197
	v_med3_f32 v107, v107, s72, v197
	v_med3_f32 v108, v108, s72, v197
	v_med3_f32 v109, v109, s72, v197
	v_med3_f32 v102, v102, s72, v197
	v_med3_f32 v103, v103, s72, v197
	v_med3_f32 v104, v104, s72, v197
	v_mfma_f32_16x16x128_f8f6f4 v[42:45], v[26:33], v[214:221], v[42:45]
	v_med3_f32 v105, v105, s72, v197
	v_med3_f32 v98, v98, s72, v197
	v_med3_f32 v99, v99, s72, v197
	v_med3_f32 v100, v100, s72, v197
	v_med3_f32 v101, v101, s72, v197
	v_cvt_pk_fp8_f32 v246, v110, v111
	v_cvt_pk_fp8_f32 v247, v106, v107
	v_mfma_f32_16x16x128_f8f6f4 v[38:41], v[18:25], v[222:229], v[38:41]
	v_cvt_pk_fp8_f32 v248, v102, v103
	v_cvt_pk_fp8_f32 v249, v98, v99
	v_add_u32_e32 v207, s73, v206
	v_add_u32_e32 v208, s74, v206
	v_cvt_pk_fp8_f32 v246, v112, v113 op_sel:[0,0,1]
	v_cvt_pk_fp8_f32 v247, v108, v109 op_sel:[0,0,1]
	v_cvt_pk_fp8_f32 v248, v104, v105 op_sel:[0,0,1]
	v_mfma_f32_16x16x128_f8f6f4 v[34:37], v[26:33], v[222:229], v[34:37]
	v_cvt_pk_fp8_f32 v249, v100, v101 op_sel:[0,0,1]
	s_nop 1
	global_store_dwordx2 v207, v[246:247], s[100:101]
	global_store_dwordx2 v208, v[248:249], s[100:101]
	s_setprio 0
	s_barrier
.Lh23_nb:
	s_nop 15
	s_nop 15
	s_branch .Lh23_epi1
.LBB0_2939:
.LBB0_2941:
	s_nop 15
	s_nop 15
	s_mul_hi_i32 s25, s81, 0x2e8ba2e9
	s_lshr_b32 s28, s25, 31
	s_lshr_b32 s25, s25, 3
	s_add_i32 s25, s25, s28
	s_mul_i32 s25, s25, 44
	s_sub_i32 s25, s81, s25
	s_lshl_b32 s28, s25, 7
	s_lshl_b32 s24, s24, 8
	s_add_i32 s24, s24, s66
	s_mul_i32 s24, s24, s71
	s_add_i32 s24, s24, s28
	s_add_i32 s24, s24, s8
	s_add_u32 s100, s12, s24
	s_addc_u32 s101, s13, 0
	s_mov_b32 s98, 0xbfb8aa3b
	v_mul_u32_u24_e32 v206, s71, v178
	v_lshl_add_u32 v206, v179, 3, v206
	v_pk_fma_f32 v[158:159], v[158:159], s[18:19], 0 op_sel_hi:[1,0,0]
	v_pk_fma_f32 v[160:161], v[160:161], s[18:19], 0 op_sel_hi:[1,0,0]
	v_pk_fma_f32 v[154:155], v[154:155], s[18:19], 0 op_sel_hi:[1,0,0]
	v_pk_fma_f32 v[156:157], v[156:157], s[18:19], 0 op_sel_hi:[1,0,0]
	v_pk_fma_f32 v[142:143], v[142:143], s[20:21], 0 op_sel_hi:[1,0,0]
	v_pk_fma_f32 v[144:145], v[144:145], s[20:21], 0 op_sel_hi:[1,0,0]
	v_pk_fma_f32 v[134:135], v[134:135], s[20:21], 0 op_sel_hi:[1,0,0]
	v_pk_fma_f32 v[136:137], v[136:137], s[20:21], 0 op_sel_hi:[1,0,0]
	v_pk_fma_f32 v[150:151], v[150:151], s[18:19], 0 op_sel_hi:[1,0,0]
	v_pk_fma_f32 v[152:153], v[152:153], s[18:19], 0 op_sel_hi:[1,0,0]
	v_pk_fma_f32 v[146:147], v[146:147], s[18:19], 0 op_sel_hi:[1,0,0]
	v_pk_fma_f32 v[148:149], v[148:149], s[18:19], 0 op_sel_hi:[1,0,0]
	v_pk_fma_f32 v[126:127], v[126:127], s[20:21], 0 op_sel_hi:[1,0,0]
	v_pk_fma_f32 v[128:129], v[128:129], s[20:21], 0 op_sel_hi:[1,0,0]
	v_pk_fma_f32 v[118:119], v[118:119], s[20:21], 0 op_sel_hi:[1,0,0]
	v_pk_fma_f32 v[120:121], v[120:121], s[20:21], 0 op_sel_hi:[1,0,0]
	v_pk_mul_f32 v[230:231], v[158:159], s[98:99] op_sel_hi:[1,0]
	v_pk_mul_f32 v[232:233], v[160:161], s[98:99] op_sel_hi:[1,0]
	v_pk_mul_f32 v[234:235], v[154:155], s[98:99] op_sel_hi:[1,0]
	v_pk_mul_f32 v[236:237], v[156:157], s[98:99] op_sel_hi:[1,0]
	v_pk_mul_f32 v[238:239], v[150:151], s[98:99] op_sel_hi:[1,0]
	v_pk_mul_f32 v[240:241], v[152:153], s[98:99] op_sel_hi:[1,0]
	v_pk_mul_f32 v[242:243], v[146:147], s[98:99] op_sel_hi:[1,0]
	v_pk_mul_f32 v[244:245], v[148:149], s[98:99] op_sel_hi:[1,0]
	v_exp_f32_e32 v230, v230
	v_exp_f32_e32 v231, v231
	v_exp_f32_e32 v232, v232
	v_exp_f32_e32 v233, v233
	v_exp_f32_e32 v234, v234
	v_exp_f32_e32 v235, v235
	v_exp_f32_e32 v236, v236
	v_exp_f32_e32 v237, v237
	v_exp_f32_e32 v238, v238
	v_exp_f32_e32 v239, v239
	v_exp_f32_e32 v240, v240
	v_exp_f32_e32 v241, v241
	v_exp_f32_e32 v242, v242
	v_exp_f32_e32 v243, v243
	v_exp_f32_e32 v244, v244
	v_exp_f32_e32 v245, v245
	v_pk_add_f32 v[230:231], v[230:231], 1.0 op_sel_hi:[1,0]
	v_pk_add_f32 v[232:233], v[232:233], 1.0 op_sel_hi:[1,0]
	v_pk_add_f32 v[234:235], v[234:235], 1.0 op_sel_hi:[1,0]
	v_pk_add_f32 v[236:237], v[236:237], 1.0 op_sel_hi:[1,0]
	v_pk_add_f32 v[238:239], v[238:239], 1.0 op_sel_hi:[1,0]
	v_pk_add_f32 v[240:241], v[240:241], 1.0 op_sel_hi:[1,0]
	v_pk_add_f32 v[242:243], v[242:243], 1.0 op_sel_hi:[1,0]
	v_pk_add_f32 v[244:245], v[244:245], 1.0 op_sel_hi:[1,0]
	v_rcp_f32_e32 v230, v230
	v_rcp_f32_e32 v231, v231
	v_rcp_f32_e32 v232, v232
	v_rcp_f32_e32 v233, v233
	v_rcp_f32_e32 v234, v234
	v_rcp_f32_e32 v235, v235
	v_rcp_f32_e32 v236, v236
	v_rcp_f32_e32 v237, v237
	v_rcp_f32_e32 v238, v238
	v_rcp_f32_e32 v239, v239
	v_rcp_f32_e32 v240, v240
	v_rcp_f32_e32 v241, v241
	v_rcp_f32_e32 v242, v242
	v_rcp_f32_e32 v243, v243
	v_rcp_f32_e32 v244, v244
	v_rcp_f32_e32 v245, v245
	v_pk_mul_f32 v[230:231], v[158:159], v[230:231]
	v_pk_mul_f32 v[232:233], v[160:161], v[232:233]
	v_pk_mul_f32 v[234:235], v[154:155], v[234:235]
	v_pk_mul_f32 v[236:237], v[156:157], v[236:237]
	v_pk_mul_f32 v[238:239], v[150:151], v[238:239]
	v_pk_mul_f32 v[240:241], v[152:153], v[240:241]
	v_pk_mul_f32 v[242:243], v[146:147], v[242:243]
	v_pk_mul_f32 v[244:245], v[148:149], v[244:245]
	v_pk_mul_f32 v[142:143], v[142:143], v[230:231]
	v_pk_mul_f32 v[144:145], v[144:145], v[232:233]
	v_pk_mul_f32 v[134:135], v[134:135], v[234:235]
	v_pk_mul_f32 v[136:137], v[136:137], v[236:237]
	v_pk_mul_f32 v[126:127], v[126:127], v[238:239]
	v_pk_mul_f32 v[128:129], v[128:129], v[240:241]
	v_pk_mul_f32 v[118:119], v[118:119], v[242:243]
	v_pk_mul_f32 v[120:121], v[120:121], v[244:245]
	v_med3_f32 v142, v142, s72, v197
	v_med3_f32 v143, v143, s72, v197
	v_med3_f32 v144, v144, s72, v197
	v_med3_f32 v145, v145, s72, v197
	v_med3_f32 v134, v134, s72, v197
	v_med3_f32 v135, v135, s72, v197
	v_med3_f32 v136, v136, s72, v197
	v_med3_f32 v137, v137, s72, v197
	v_med3_f32 v126, v126, s72, v197
	v_med3_f32 v127, v127, s72, v197
	v_med3_f32 v128, v128, s72, v197
	v_med3_f32 v129, v129, s72, v197
	v_med3_f32 v118, v118, s72, v197
	v_med3_f32 v119, v119, s72, v197
	v_med3_f32 v120, v120, s72, v197
	v_med3_f32 v121, v121, s72, v197
	v_cvt_pk_fp8_f32 v246, v142, v143
	v_cvt_pk_fp8_f32 v247, v134, v135
	v_cvt_pk_fp8_f32 v248, v126, v127
	v_cvt_pk_fp8_f32 v249, v118, v119
	v_add_u32_e32 v208, s57, v206
	v_cvt_pk_fp8_f32 v246, v144, v145 op_sel:[0,0,1]
	v_cvt_pk_fp8_f32 v247, v136, v137 op_sel:[0,0,1]
	v_cvt_pk_fp8_f32 v248, v128, v129 op_sel:[0,0,1]
	v_cvt_pk_fp8_f32 v249, v120, v121 op_sel:[0,0,1]
	s_nop 1
	global_store_dwordx2 v206, v[246:247], s[100:101]
	global_store_dwordx2 v208, v[248:249], s[100:101]
	v_pk_fma_f32 v[138:139], v[138:139], s[18:19], 0 op_sel_hi:[1,0,0]
	v_pk_fma_f32 v[140:141], v[140:141], s[18:19], 0 op_sel_hi:[1,0,0]
	v_pk_fma_f32 v[130:131], v[130:131], s[18:19], 0 op_sel_hi:[1,0,0]
	v_pk_fma_f32 v[132:133], v[132:133], s[18:19], 0 op_sel_hi:[1,0,0]
	v_pk_fma_f32 v[110:111], v[110:111], s[20:21], 0 op_sel_hi:[1,0,0]
	v_pk_fma_f32 v[112:113], v[112:113], s[20:21], 0 op_sel_hi:[1,0,0]
	v_pk_fma_f32 v[106:107], v[106:107], s[20:21], 0 op_sel_hi:[1,0,0]
	v_pk_fma_f32 v[108:109], v[108:109], s[20:21], 0 op_sel_hi:[1,0,0]
	v_pk_fma_f32 v[122:123], v[122:123], s[18:19], 0 op_sel_hi:[1,0,0]
	v_pk_fma_f32 v[124:125], v[124:125], s[18:19], 0 op_sel_hi:[1,0,0]
	v_pk_fma_f32 v[114:115], v[114:115], s[18:19], 0 op_sel_hi:[1,0,0]
	v_pk_fma_f32 v[116:117], v[116:117], s[18:19], 0 op_sel_hi:[1,0,0]
	v_pk_fma_f32 v[102:103], v[102:103], s[20:21], 0 op_sel_hi:[1,0,0]
	v_pk_fma_f32 v[104:105], v[104:105], s[20:21], 0 op_sel_hi:[1,0,0]
	v_pk_fma_f32 v[98:99], v[98:99], s[20:21], 0 op_sel_hi:[1,0,0]
	v_pk_fma_f32 v[100:101], v[100:101], s[20:21], 0 op_sel_hi:[1,0,0]
	v_pk_mul_f32 v[230:231], v[138:139], s[98:99] op_sel_hi:[1,0]
	v_pk_mul_f32 v[232:233], v[140:141], s[98:99] op_sel_hi:[1,0]
	v_pk_mul_f32 v[234:235], v[130:131], s[98:99] op_sel_hi:[1,0]
	v_pk_mul_f32 v[236:237], v[132:133], s[98:99] op_sel_hi:[1,0]
	v_pk_mul_f32 v[238:239], v[122:123], s[98:99] op_sel_hi:[1,0]
	v_pk_mul_f32 v[240:241], v[124:125], s[98:99] op_sel_hi:[1,0]
	v_pk_mul_f32 v[242:243], v[114:115], s[98:99] op_sel_hi:[1,0]
	v_pk_mul_f32 v[244:245], v[116:117], s[98:99] op_sel_hi:[1,0]
	v_exp_f32_e32 v230, v230
	v_exp_f32_e32 v231, v231
	v_exp_f32_e32 v232, v232
	v_exp_f32_e32 v233, v233
	v_exp_f32_e32 v234, v234
	v_exp_f32_e32 v235, v235
	v_exp_f32_e32 v236, v236
	v_exp_f32_e32 v237, v237
	v_exp_f32_e32 v238, v238
	v_exp_f32_e32 v239, v239
	v_exp_f32_e32 v240, v240
	v_exp_f32_e32 v241, v241
	v_exp_f32_e32 v242, v242
	v_exp_f32_e32 v243, v243
	v_exp_f32_e32 v244, v244
	v_exp_f32_e32 v245, v245
	v_pk_add_f32 v[230:231], v[230:231], 1.0 op_sel_hi:[1,0]
	v_pk_add_f32 v[232:233], v[232:233], 1.0 op_sel_hi:[1,0]
	v_pk_add_f32 v[234:235], v[234:235], 1.0 op_sel_hi:[1,0]
	v_pk_add_f32 v[236:237], v[236:237], 1.0 op_sel_hi:[1,0]
	v_pk_add_f32 v[238:239], v[238:239], 1.0 op_sel_hi:[1,0]
	v_pk_add_f32 v[240:241], v[240:241], 1.0 op_sel_hi:[1,0]
	v_pk_add_f32 v[242:243], v[242:243], 1.0 op_sel_hi:[1,0]
	v_pk_add_f32 v[244:245], v[244:245], 1.0 op_sel_hi:[1,0]
	v_rcp_f32_e32 v230, v230
	v_rcp_f32_e32 v231, v231
	v_rcp_f32_e32 v232, v232
	v_rcp_f32_e32 v233, v233
	v_rcp_f32_e32 v234, v234
	v_rcp_f32_e32 v235, v235
	v_rcp_f32_e32 v236, v236
	v_rcp_f32_e32 v237, v237
	v_rcp_f32_e32 v238, v238
	v_rcp_f32_e32 v239, v239
	v_rcp_f32_e32 v240, v240
	v_rcp_f32_e32 v241, v241
	v_rcp_f32_e32 v242, v242
	v_rcp_f32_e32 v243, v243
	v_rcp_f32_e32 v244, v244
	v_rcp_f32_e32 v245, v245
	v_pk_mul_f32 v[230:231], v[138:139], v[230:231]
	v_pk_mul_f32 v[232:233], v[140:141], v[232:233]
	v_pk_mul_f32 v[234:235], v[130:131], v[234:235]
	v_pk_mul_f32 v[236:237], v[132:133], v[236:237]
	v_pk_mul_f32 v[238:239], v[122:123], v[238:239]
	v_pk_mul_f32 v[240:241], v[124:125], v[240:241]
	v_pk_mul_f32 v[242:243], v[114:115], v[242:243]
	v_pk_mul_f32 v[244:245], v[116:117], v[244:245]
	v_pk_mul_f32 v[110:111], v[110:111], v[230:231]
	v_pk_mul_f32 v[112:113], v[112:113], v[232:233]
	v_pk_mul_f32 v[106:107], v[106:107], v[234:235]
	v_pk_mul_f32 v[108:109], v[108:109], v[236:237]
	v_pk_mul_f32 v[102:103], v[102:103], v[238:239]
	v_pk_mul_f32 v[104:105], v[104:105], v[240:241]
	v_pk_mul_f32 v[98:99], v[98:99], v[242:243]
	v_pk_mul_f32 v[100:101], v[100:101], v[244:245]
	v_med3_f32 v110, v110, s72, v197
	v_med3_f32 v111, v111, s72, v197
	v_med3_f32 v112, v112, s72, v197
	v_med3_f32 v113, v113, s72, v197
	v_med3_f32 v106, v106, s72, v197
	v_med3_f32 v107, v107, s72, v197
	v_med3_f32 v108, v108, s72, v197
	v_med3_f32 v109, v109, s72, v197
	v_med3_f32 v102, v102, s72, v197
	v_med3_f32 v103, v103, s72, v197
	v_med3_f32 v104, v104, s72, v197
	v_med3_f32 v105, v105, s72, v197
	v_med3_f32 v98, v98, s72, v197
	v_med3_f32 v99, v99, s72, v197
	v_med3_f32 v100, v100, s72, v197
	v_med3_f32 v101, v101, s72, v197
	v_cvt_pk_fp8_f32 v250, v110, v111
	v_cvt_pk_fp8_f32 v251, v106, v107
	v_cvt_pk_fp8_f32 v252, v102, v103
	v_cvt_pk_fp8_f32 v253, v98, v99
	v_add_u32_e32 v207, s73, v206
	v_add_u32_e32 v208, s74, v206
	v_cvt_pk_fp8_f32 v250, v112, v113 op_sel:[0,0,1]
	v_cvt_pk_fp8_f32 v251, v108, v109 op_sel:[0,0,1]
	v_cvt_pk_fp8_f32 v252, v104, v105 op_sel:[0,0,1]
	v_cvt_pk_fp8_f32 v253, v100, v101 op_sel:[0,0,1]
	s_nop 1
	global_store_dwordx2 v207, v[250:251], s[100:101]
	global_store_dwordx2 v208, v[252:253], s[100:101]
.Lh23_epi1:
	v_pk_fma_f32 v[94:95], v[94:95], s[18:19], 0 op_sel_hi:[1,0,0]
	v_pk_fma_f32 v[96:97], v[96:97], s[18:19], 0 op_sel_hi:[1,0,0]
	v_pk_fma_f32 v[90:91], v[90:91], s[18:19], 0 op_sel_hi:[1,0,0]
	v_pk_fma_f32 v[92:93], v[92:93], s[18:19], 0 op_sel_hi:[1,0,0]
	v_pk_fma_f32 v[78:79], v[78:79], s[20:21], 0 op_sel_hi:[1,0,0]
	v_pk_fma_f32 v[80:81], v[80:81], s[20:21], 0 op_sel_hi:[1,0,0]
	v_pk_fma_f32 v[70:71], v[70:71], s[20:21], 0 op_sel_hi:[1,0,0]
	v_pk_fma_f32 v[72:73], v[72:73], s[20:21], 0 op_sel_hi:[1,0,0]
	v_pk_fma_f32 v[86:87], v[86:87], s[18:19], 0 op_sel_hi:[1,0,0]
	v_pk_fma_f32 v[88:89], v[88:89], s[18:19], 0 op_sel_hi:[1,0,0]
	v_pk_fma_f32 v[82:83], v[82:83], s[18:19], 0 op_sel_hi:[1,0,0]
	v_pk_fma_f32 v[84:85], v[84:85], s[18:19], 0 op_sel_hi:[1,0,0]
	v_pk_fma_f32 v[62:63], v[62:63], s[20:21], 0 op_sel_hi:[1,0,0]
	v_pk_fma_f32 v[64:65], v[64:65], s[20:21], 0 op_sel_hi:[1,0,0]
	v_pk_fma_f32 v[54:55], v[54:55], s[20:21], 0 op_sel_hi:[1,0,0]
	v_pk_fma_f32 v[56:57], v[56:57], s[20:21], 0 op_sel_hi:[1,0,0]
	v_pk_mul_f32 v[230:231], v[94:95], s[98:99] op_sel_hi:[1,0]
	v_pk_mul_f32 v[232:233], v[96:97], s[98:99] op_sel_hi:[1,0]
	v_pk_mul_f32 v[234:235], v[90:91], s[98:99] op_sel_hi:[1,0]
	v_pk_mul_f32 v[236:237], v[92:93], s[98:99] op_sel_hi:[1,0]
	v_pk_mul_f32 v[238:239], v[86:87], s[98:99] op_sel_hi:[1,0]
	v_pk_mul_f32 v[240:241], v[88:89], s[98:99] op_sel_hi:[1,0]
	v_pk_mul_f32 v[242:243], v[82:83], s[98:99] op_sel_hi:[1,0]
	v_pk_mul_f32 v[244:245], v[84:85], s[98:99] op_sel_hi:[1,0]
	v_exp_f32_e32 v230, v230
	v_exp_f32_e32 v231, v231
	v_exp_f32_e32 v232, v232
	v_exp_f32_e32 v233, v233
	v_exp_f32_e32 v234, v234
	v_exp_f32_e32 v235, v235
	v_exp_f32_e32 v236, v236
	v_exp_f32_e32 v237, v237
	v_exp_f32_e32 v238, v238
	v_exp_f32_e32 v239, v239
	v_exp_f32_e32 v240, v240
	v_exp_f32_e32 v241, v241
	v_exp_f32_e32 v242, v242
	v_exp_f32_e32 v243, v243
	v_exp_f32_e32 v244, v244
	v_exp_f32_e32 v245, v245
	v_pk_add_f32 v[230:231], v[230:231], 1.0 op_sel_hi:[1,0]
	v_pk_add_f32 v[232:233], v[232:233], 1.0 op_sel_hi:[1,0]
	v_pk_add_f32 v[234:235], v[234:235], 1.0 op_sel_hi:[1,0]
	v_pk_add_f32 v[236:237], v[236:237], 1.0 op_sel_hi:[1,0]
	v_pk_add_f32 v[238:239], v[238:239], 1.0 op_sel_hi:[1,0]
	v_pk_add_f32 v[240:241], v[240:241], 1.0 op_sel_hi:[1,0]
	v_pk_add_f32 v[242:243], v[242:243], 1.0 op_sel_hi:[1,0]
	v_pk_add_f32 v[244:245], v[244:245], 1.0 op_sel_hi:[1,0]
	v_rcp_f32_e32 v230, v230
	v_rcp_f32_e32 v231, v231
	v_rcp_f32_e32 v232, v232
	v_rcp_f32_e32 v233, v233
	v_rcp_f32_e32 v234, v234
	v_rcp_f32_e32 v235, v235
	v_rcp_f32_e32 v236, v236
	v_rcp_f32_e32 v237, v237
	v_rcp_f32_e32 v238, v238
	v_rcp_f32_e32 v239, v239
	v_rcp_f32_e32 v240, v240
	v_rcp_f32_e32 v241, v241
	v_rcp_f32_e32 v242, v242
	v_rcp_f32_e32 v243, v243
	v_rcp_f32_e32 v244, v244
	v_rcp_f32_e32 v245, v245
	v_pk_mul_f32 v[230:231], v[94:95], v[230:231]
	v_pk_mul_f32 v[232:233], v[96:97], v[232:233]
	v_pk_mul_f32 v[234:235], v[90:91], v[234:235]
	v_pk_mul_f32 v[236:237], v[92:93], v[236:237]
	v_pk_mul_f32 v[238:239], v[86:87], v[238:239]
	v_pk_mul_f32 v[240:241], v[88:89], v[240:241]
	v_pk_mul_f32 v[242:243], v[82:83], v[242:243]
	v_pk_mul_f32 v[244:245], v[84:85], v[244:245]
	v_pk_mul_f32 v[78:79], v[78:79], v[230:231]
	v_pk_mul_f32 v[80:81], v[80:81], v[232:233]
	v_pk_mul_f32 v[70:71], v[70:71], v[234:235]
	v_pk_mul_f32 v[72:73], v[72:73], v[236:237]
	v_pk_mul_f32 v[62:63], v[62:63], v[238:239]
	v_pk_mul_f32 v[64:65], v[64:65], v[240:241]
	v_pk_mul_f32 v[54:55], v[54:55], v[242:243]
	v_pk_mul_f32 v[56:57], v[56:57], v[244:245]
	v_med3_f32 v78, v78, s72, v197
	v_med3_f32 v79, v79, s72, v197
	v_med3_f32 v80, v80, s72, v197
	v_med3_f32 v81, v81, s72, v197
	v_med3_f32 v70, v70, s72, v197
	v_med3_f32 v71, v71, s72, v197
	v_med3_f32 v72, v72, s72, v197
	v_med3_f32 v73, v73, s72, v197
	v_med3_f32 v62, v62, s72, v197
	v_med3_f32 v63, v63, s72, v197
	v_med3_f32 v64, v64, s72, v197
	v_med3_f32 v65, v65, s72, v197
	v_med3_f32 v54, v54, s72, v197
	v_med3_f32 v55, v55, s72, v197
	v_med3_f32 v56, v56, s72, v197
	v_med3_f32 v57, v57, s72, v197
	v_cvt_pk_fp8_f32 v246, v78, v79
	v_cvt_pk_fp8_f32 v247, v70, v71
	v_cvt_pk_fp8_f32 v248, v62, v63
	v_cvt_pk_fp8_f32 v249, v54, v55
	v_add_u32_e32 v207, s75, v206
	v_add_u32_e32 v208, s76, v206
	v_cvt_pk_fp8_f32 v246, v80, v81 op_sel:[0,0,1]
	v_cvt_pk_fp8_f32 v247, v72, v73 op_sel:[0,0,1]
	v_cvt_pk_fp8_f32 v248, v64, v65 op_sel:[0,0,1]
	v_cvt_pk_fp8_f32 v249, v56, v57 op_sel:[0,0,1]
	s_nop 1
	global_store_dwordx2 v207, v[246:247], s[100:101]
	global_store_dwordx2 v208, v[248:249], s[100:101]
	v_pk_fma_f32 v[74:75], v[74:75], s[18:19], 0 op_sel_hi:[1,0,0]
	v_pk_fma_f32 v[76:77], v[76:77], s[18:19], 0 op_sel_hi:[1,0,0]
	v_pk_fma_f32 v[66:67], v[66:67], s[18:19], 0 op_sel_hi:[1,0,0]
	v_pk_fma_f32 v[68:69], v[68:69], s[18:19], 0 op_sel_hi:[1,0,0]
	v_pk_fma_f32 v[46:47], v[46:47], s[20:21], 0 op_sel_hi:[1,0,0]
	v_pk_fma_f32 v[48:49], v[48:49], s[20:21], 0 op_sel_hi:[1,0,0]
	v_pk_fma_f32 v[42:43], v[42:43], s[20:21], 0 op_sel_hi:[1,0,0]
	v_pk_fma_f32 v[44:45], v[44:45], s[20:21], 0 op_sel_hi:[1,0,0]
	v_pk_fma_f32 v[58:59], v[58:59], s[18:19], 0 op_sel_hi:[1,0,0]
	v_pk_fma_f32 v[60:61], v[60:61], s[18:19], 0 op_sel_hi:[1,0,0]
	v_pk_fma_f32 v[50:51], v[50:51], s[18:19], 0 op_sel_hi:[1,0,0]
	v_pk_fma_f32 v[52:53], v[52:53], s[18:19], 0 op_sel_hi:[1,0,0]
	v_pk_fma_f32 v[38:39], v[38:39], s[20:21], 0 op_sel_hi:[1,0,0]
	v_pk_fma_f32 v[40:41], v[40:41], s[20:21], 0 op_sel_hi:[1,0,0]
	v_pk_fma_f32 v[34:35], v[34:35], s[20:21], 0 op_sel_hi:[1,0,0]
	v_pk_fma_f32 v[36:37], v[36:37], s[20:21], 0 op_sel_hi:[1,0,0]
	v_pk_mul_f32 v[230:231], v[74:75], s[98:99] op_sel_hi:[1,0]
	v_pk_mul_f32 v[232:233], v[76:77], s[98:99] op_sel_hi:[1,0]
	v_pk_mul_f32 v[234:235], v[66:67], s[98:99] op_sel_hi:[1,0]
	v_pk_mul_f32 v[236:237], v[68:69], s[98:99] op_sel_hi:[1,0]
	v_pk_mul_f32 v[238:239], v[58:59], s[98:99] op_sel_hi:[1,0]
	v_pk_mul_f32 v[240:241], v[60:61], s[98:99] op_sel_hi:[1,0]
	v_pk_mul_f32 v[242:243], v[50:51], s[98:99] op_sel_hi:[1,0]
	v_pk_mul_f32 v[244:245], v[52:53], s[98:99] op_sel_hi:[1,0]
	v_exp_f32_e32 v230, v230
	v_exp_f32_e32 v231, v231
	v_exp_f32_e32 v232, v232
	v_exp_f32_e32 v233, v233
	v_exp_f32_e32 v234, v234
	v_exp_f32_e32 v235, v235
	v_exp_f32_e32 v236, v236
	v_exp_f32_e32 v237, v237
	v_exp_f32_e32 v238, v238
	v_exp_f32_e32 v239, v239
	v_exp_f32_e32 v240, v240
	v_exp_f32_e32 v241, v241
	v_exp_f32_e32 v242, v242
	v_exp_f32_e32 v243, v243
	v_exp_f32_e32 v244, v244
	v_exp_f32_e32 v245, v245
	v_pk_add_f32 v[230:231], v[230:231], 1.0 op_sel_hi:[1,0]
	v_pk_add_f32 v[232:233], v[232:233], 1.0 op_sel_hi:[1,0]
	v_pk_add_f32 v[234:235], v[234:235], 1.0 op_sel_hi:[1,0]
	v_pk_add_f32 v[236:237], v[236:237], 1.0 op_sel_hi:[1,0]
	v_pk_add_f32 v[238:239], v[238:239], 1.0 op_sel_hi:[1,0]
	v_pk_add_f32 v[240:241], v[240:241], 1.0 op_sel_hi:[1,0]
	v_pk_add_f32 v[242:243], v[242:243], 1.0 op_sel_hi:[1,0]
	v_pk_add_f32 v[244:245], v[244:245], 1.0 op_sel_hi:[1,0]
	v_rcp_f32_e32 v230, v230
	v_rcp_f32_e32 v231, v231
	v_rcp_f32_e32 v232, v232
	v_rcp_f32_e32 v233, v233
	v_rcp_f32_e32 v234, v234
	v_rcp_f32_e32 v235, v235
	v_rcp_f32_e32 v236, v236
	v_rcp_f32_e32 v237, v237
	v_rcp_f32_e32 v238, v238
	v_rcp_f32_e32 v239, v239
	v_rcp_f32_e32 v240, v240
	v_rcp_f32_e32 v241, v241
	v_rcp_f32_e32 v242, v242
	v_rcp_f32_e32 v243, v243
	v_rcp_f32_e32 v244, v244
	v_rcp_f32_e32 v245, v245
	v_pk_mul_f32 v[230:231], v[74:75], v[230:231]
	v_pk_mul_f32 v[232:233], v[76:77], v[232:233]
	v_pk_mul_f32 v[234:235], v[66:67], v[234:235]
	v_pk_mul_f32 v[236:237], v[68:69], v[236:237]
	v_pk_mul_f32 v[238:239], v[58:59], v[238:239]
	v_pk_mul_f32 v[240:241], v[60:61], v[240:241]
	v_pk_mul_f32 v[242:243], v[50:51], v[242:243]
	v_pk_mul_f32 v[244:245], v[52:53], v[244:245]
	v_pk_mul_f32 v[46:47], v[46:47], v[230:231]
	v_pk_mul_f32 v[48:49], v[48:49], v[232:233]
	v_pk_mul_f32 v[42:43], v[42:43], v[234:235]
	v_pk_mul_f32 v[44:45], v[44:45], v[236:237]
	v_pk_mul_f32 v[38:39], v[38:39], v[238:239]
	v_pk_mul_f32 v[40:41], v[40:41], v[240:241]
	v_pk_mul_f32 v[34:35], v[34:35], v[242:243]
	v_pk_mul_f32 v[36:37], v[36:37], v[244:245]
	v_med3_f32 v46, v46, s72, v197
	v_med3_f32 v47, v47, s72, v197
	v_med3_f32 v48, v48, s72, v197
	v_med3_f32 v49, v49, s72, v197
	v_med3_f32 v42, v42, s72, v197
	v_med3_f32 v43, v43, s72, v197
	v_med3_f32 v44, v44, s72, v197
	v_med3_f32 v45, v45, s72, v197
	v_med3_f32 v38, v38, s72, v197
	v_med3_f32 v39, v39, s72, v197
	v_med3_f32 v40, v40, s72, v197
	v_med3_f32 v41, v41, s72, v197
	v_med3_f32 v34, v34, s72, v197
	v_med3_f32 v35, v35, s72, v197
	v_med3_f32 v36, v36, s72, v197
	v_med3_f32 v37, v37, s72, v197
	v_cvt_pk_fp8_f32 v250, v46, v47
	v_cvt_pk_fp8_f32 v251, v42, v43
	v_cvt_pk_fp8_f32 v252, v38, v39
	v_cvt_pk_fp8_f32 v253, v34, v35
	v_add_u32_e32 v207, s77, v206
	v_add_u32_e32 v208, 0xf2000, v206
	v_cvt_pk_fp8_f32 v250, v48, v49 op_sel:[0,0,1]
	v_cvt_pk_fp8_f32 v251, v44, v45 op_sel:[0,0,1]
	v_cvt_pk_fp8_f32 v252, v40, v41 op_sel:[0,0,1]
	v_cvt_pk_fp8_f32 v253, v36, v37 op_sel:[0,0,1]
	s_nop 1
	global_store_dwordx2 v207, v[250:251], s[100:101]
	global_store_dwordx2 v208, v[252:253], s[100:101]
	s_andn2_b64 vcc, exec, s[2:3]
	s_mov_b64 s[2:3], -1
	s_cbranch_vccnz .LBB0_2928
	s_branch .LBB0_2927
.LBB0_2944:
	s_and_b64 vcc, exec, s[16:17]
	s_cbranch_vccz .Lna23_end
	s_barrier
.Lna23_end:
	s_waitcnt vmcnt(0)
	s_barrier
